# PEER: wave-major static token assignment (token = wave*gridDim + block, stride 8*gridDim) replaces the tail-round remap; same 66 tokens per workgroup
# speedup vs baseline: 1.0245x; 1.0000x over previous
.LBB0_709:
	s_mul_i32 s8, s6, 0xab
	s_bfe_u32 s8, s8, 0x70009
	s_mul_i32 s8, s8, 3
	s_add_i32 s9, s6, -3
	s_sub_i32 s37, s6, s8
	s_cmp_lt_u32 s9, 3
	s_cselect_b32 s42, 0, 0x800
	s_cmp_gt_u32 s6, 2
	s_cselect_b64 s[8:9], -1, 0
	s_and_b64 s[40:41], s[8:9], exec
	s_cselect_b32 s40, s42, 0x2800
	s_and_b64 s[8:9], s[96:97], s[8:9]
	v_cndmask_b32_e64 v8, 0, 1, s[8:9]
	s_and_b32 s8, s37, 0xff
	v_readfirstlane_b32 s9, v8
	s_add_i32 s9, s36, s9
	s_mul_i32 s9, s9, 3
	s_add_i32 s8, s9, s8
	s_mul_hi_u32 s9, s8, 0xc000
	s_mul_i32 s8, s8, 0xc000
	s_add_u32 s8, s4, s8
	s_addc_u32 s9, s5, s9
	s_lshl_b32 s37, s40, 2
	s_add_u32 s8, s8, s37
	s_addc_u32 s9, s9, 0
	v_lshl_add_u64 v[8:9], v[4:5], 2, s[8:9]
	global_load_dwordx4 v[8:11], v[8:9], off
	s_add_i32 s6, s6, 1
	s_cmp_eq_u32 s6, 9
	s_waitcnt vmcnt(0)
	ds_write_b128 v7, v[8:11]
	v_add_u32_e32 v7, 0x2000, v7
	s_cbranch_scc0 .LBB0_709
	s_load_dwordx4 s[40:43], s[0:1], 0x90
	s_lshl_b32 s6, s36, 11
	s_lshl_b64 s[4:5], s[6:7], 2
	v_lshlrev_b64 v[8:9], 2, v[4:5]
	v_add_u32_e32 v10, 0, v6
	s_waitcnt lgkmcnt(0)
	s_add_u32 s8, s40, s4
	s_addc_u32 s9, s41, s5
	v_lshl_add_u64 v[4:5], s[8:9], 0, v[8:9]
	global_load_dwordx4 v[4:7], v[4:5], off
	s_add_u32 s4, s42, s4
	v_add_u32_e32 v11, 0x1c200, v10
	s_addc_u32 s5, s43, s5
	s_lshl_b32 s6, s36, 6
	v_and_b32_e32 v21, 63, v2
	v_cmp_eq_u32_e64 s[40:41], 0, v21
	s_waitcnt vmcnt(0)
	ds_write_b128 v11, v[4:7]
	v_lshl_add_u64 v[4:5], s[4:5], 0, v[8:9]
	global_load_dwordx4 v[4:7], v[4:5], off
	s_lshl_b64 s[4:5], s[6:7], 2
	v_readlane_b32 s6, v254, 50
	v_add_u32_e32 v8, 0x1e200, v10
	s_add_u32 s66, s6, s4
	v_readlane_b32 s4, v254, 51
	s_addc_u32 s67, s4, s5
	s_waitcnt vmcnt(0)
	ds_write_b128 v8, v[4:7]
	v_mov_b32_e32 v4, 0
	s_waitcnt lgkmcnt(0)
	s_barrier
	s_lshr_b32 s4, s27, 6
	s_mul_i32 s4, s4, s33
	s_add_i32 s6, s4, s2
	s_nop 0
	v_readlane_b32 s44, v253, 31
	v_readlane_b32 s45, v253, 32
	s_mov_b32 s88, s6
	s_cmp_lt_i32 s88, s26
	v_lshlrev_b32_e32 v20, 6, v21
	s_cselect_b64 s[4:5], -1, 0
	s_cmp_ge_i32 s88, s26
	v_and_b32_e32 v24, 0xf00, v20
	v_and_b32_e32 v22, 0xc0, v20
	s_cbranch_scc1 .LBB0_716
	s_ashr_i32 s89, s88, 31
	s_lshl_b64 s[8:9], s[88:89], 12
	s_add_u32 s8, s50, s8
	s_addc_u32 s9, s51, s9
	v_mov_b32_e32 v25, v3
	v_lshl_add_u64 v[4:5], s[8:9], 0, v[24:25]
	v_mov_b32_e32 v23, v3
	v_lshl_add_u64 v[4:5], v[4:5], 0, v[22:23]
	s_mov_b64 s[8:9], 0x24d00000
	s_mov_b32 s6, 0x24d00000
	v_lshl_add_u64 v[16:17], v[4:5], 0, s[8:9]
	v_add_co_u32_e32 v4, vcc, s6, v4
	s_nop 1
	v_addc_co_u32_e32 v5, vcc, 0, v5, vcc
	global_load_dwordx4 v[4:7], v[4:5], off
	s_nop 0
	global_load_dwordx4 v[8:11], v[16:17], off offset:48
	global_load_dwordx4 v[12:15], v[16:17], off offset:32
	s_nop 0
	global_load_dwordx4 v[16:19], v[16:17], off offset:16
